# P0 g*w_xq bf16 copy: all 10-11 per-thread loads issued as one batch, counted waits (strategy 2), on top of best
# speedup vs baseline: 1.0179x; 1.0179x over previous
; #define GAS __attribute__((address_space(1)))
; __device__ __forceinline__ unsigned pk2(float lo, float hi) { return f2bf(lo) | (f2bf(hi) << 16); }
; __global__ void __launch_bounds__(NTHR, 2) fwd(Args args) {
;     ...
;         if (bx < G) { s5_setup(bx, lds, INP(9), INP(10), INP(11), INP(12), INP(13), INP(14), INP(15), WSP(bf16, WS_BTY), WSP(bf16, WS_BTS), WSP(float, WS_AP32), tid); }
;         else {
;             const int gw = (bx - G) * NWAVES + wave, NGW = (NG - G) * NWAVES, gt = (bx - G) * NTHR + tid, NGT = (NG - G) * NTHR;
;             for (int i = gt; i < D * D / 4; i += NGT) { const int row = (i * 4) / D; const f32x4 w = ((const GAS f32x4*)INP(24))[i]; const float g = INP(22)[row]; v2u o; o.x = pk2(w.x * g, w.y * g); o.y = pk2(w.z * g, w.w * g);
;                 ((GAS v2u*)WSP(bf16, WS_WXQN))[i] = o; }
.LBB0_10:
	s_waitcnt lgkmcnt(0)
	v_writelane_b32 v254, s44, 42
	s_add_u32 s88, s78, 0x37dc8000
	s_addc_u32 s87, s79, 0
	v_writelane_b32 v254, s45, 43
	v_writelane_b32 v254, s46, 44
	v_writelane_b32 v254, s47, 45
	v_writelane_b32 v254, s48, 46
	v_writelane_b32 v254, s49, 47
	v_writelane_b32 v254, s50, 48
	v_writelane_b32 v254, s51, 49
	v_writelane_b32 v254, s52, 50
	s_add_u32 s90, s78, 0x10000
	v_writelane_b32 v254, s53, 51
	s_addc_u32 s91, s79, 0
	v_writelane_b32 v254, s54, 52
	s_cmp_gt_i32 s80, 0
	v_writelane_b32 v254, s55, 53
	s_cselect_b64 s[0:1], -1, 0
	s_cmp_lt_i32 s81, 1
	v_writelane_b32 v254, s56, 54
	s_cselect_b64 s[2:3], -1, 0
	v_writelane_b32 v254, s57, 55
	s_or_b64 s[0:1], s[0:1], s[2:3]
	v_writelane_b32 v254, s58, 56
	s_and_b64 vcc, exec, s[0:1]
	v_writelane_b32 v254, s59, 57
	s_cbranch_vccnz .LBB0_264
	v_mov_b32_e32 v0, 0
	s_cmp_gt_i32 s92, 63
	v_mbcnt_lo_u32_b32 v0, -1, v0
	v_mbcnt_hi_u32_b32 v134, -1, v0
	s_mov_b64 s[0:1], -1
	v_add_u32_e32 v132, s94, v134
	s_cbranch_scc0 .LBB0_22
	s_sub_i32 s3, s92, 64
	s_sub_i32 s2, s83, 64
	v_lshl_add_u32 v136, s3, 9, v132
	s_mov_b32 s0, 0x100000
	s_lshl_b32 s24, s2, 9
	v_cmp_gt_i32_e32 vcc, s0, v136
	v_ashrrev_i32_e32 v137, 31, v136
	s_and_saveexec_b64 s[0:1], vcc
	v_readlane_b32 s60, v254, 26
	v_readlane_b32 s72, v254, 38
	v_readlane_b32 s73, v254, 39
	v_readlane_b32 s61, v254, 27
	v_readlane_b32 s62, v254, 28
	v_readlane_b32 s63, v254, 29
	v_readlane_b32 s64, v254, 30
	v_readlane_b32 s65, v254, 31
	v_readlane_b32 s66, v254, 32
	v_readlane_b32 s67, v254, 33
	v_readlane_b32 s68, v254, 34
	v_readlane_b32 s69, v254, 35
	v_readlane_b32 s70, v254, 36
	v_readlane_b32 s71, v254, 37
	v_readlane_b32 s74, v254, 40
	v_readlane_b32 s75, v254, 41
	s_cbranch_execz .LBB0_15
	v_lshlrev_b32_e32 v0, 4, v136
	v_lshlrev_b32_e32 v1, 3, v136
	v_lshrrev_b32_e32 v2, 9, v136
	v_lshlrev_b32_e32 v2, 2, v2
	s_mov_b64 s[4:5], s[44:45]
	s_mov_b64 s[6:7], s[72:73]
	s_add_u32 s26, s78, 0x18c28000
	s_addc_u32 s27, s79, 0
	s_movk_i32 s25, 0x7fff
	s_mov_b32 s28, 0xffff0000
	global_load_dwordx4 v[8:11], v0, s[4:5]
	global_load_dword v56, v2, s[6:7]
	s_add_u32 s4, s4, 0x180000
	s_addc_u32 s5, s5, 0
	s_add_u32 s6, s6, 0x300
	s_addc_u32 s7, s7, 0
	global_load_dwordx4 v[12:15], v0, s[4:5]
	global_load_dword v58, v2, s[6:7]
	s_add_u32 s4, s4, 0x180000
	s_addc_u32 s5, s5, 0
	s_add_u32 s6, s6, 0x300
	s_addc_u32 s7, s7, 0
	global_load_dwordx4 v[16:19], v0, s[4:5]
	global_load_dword v60, v2, s[6:7]
	s_add_u32 s4, s4, 0x180000
	s_addc_u32 s5, s5, 0
	s_add_u32 s6, s6, 0x300
	s_addc_u32 s7, s7, 0
	global_load_dwordx4 v[20:23], v0, s[4:5]
	global_load_dword v62, v2, s[6:7]
	s_add_u32 s4, s4, 0x180000
	s_addc_u32 s5, s5, 0
	s_add_u32 s6, s6, 0x300
	s_addc_u32 s7, s7, 0
	global_load_dwordx4 v[24:27], v0, s[4:5]
	global_load_dword v64, v2, s[6:7]
	s_add_u32 s4, s4, 0x180000
	s_addc_u32 s5, s5, 0
	s_add_u32 s6, s6, 0x300
	s_addc_u32 s7, s7, 0
	global_load_dwordx4 v[28:31], v0, s[4:5]
	global_load_dword v66, v2, s[6:7]
	s_add_u32 s4, s4, 0x180000
	s_addc_u32 s5, s5, 0
	s_add_u32 s6, s6, 0x300
	s_addc_u32 s7, s7, 0
	global_load_dwordx4 v[32:35], v0, s[4:5]
	global_load_dword v68, v2, s[6:7]
	s_add_u32 s4, s4, 0x180000
	s_addc_u32 s5, s5, 0
	s_add_u32 s6, s6, 0x300
	s_addc_u32 s7, s7, 0
	global_load_dwordx4 v[36:39], v0, s[4:5]
	global_load_dword v70, v2, s[6:7]
	s_add_u32 s4, s4, 0x180000
	s_addc_u32 s5, s5, 0
	s_add_u32 s6, s6, 0x300
	s_addc_u32 s7, s7, 0
	global_load_dwordx4 v[40:43], v0, s[4:5]
	global_load_dword v72, v2, s[6:7]
	s_add_u32 s4, s4, 0x180000
	s_addc_u32 s5, s5, 0
	s_add_u32 s6, s6, 0x300
	s_addc_u32 s7, s7, 0
	global_load_dwordx4 v[44:47], v0, s[4:5]
	global_load_dword v74, v2, s[6:7]
	s_add_u32 s4, s4, 0x180000
	s_addc_u32 s5, s5, 0
	s_add_u32 s6, s6, 0x300
	s_addc_u32 s7, s7, 0
	s_cmp_lt_u32 s3, 128
	s_cbranch_scc0 .Lxq_no11a
	global_load_dwordx4 v[48:51], v0, s[4:5]
	global_load_dword v76, v2, s[6:7]
	s_add_u32 s4, s4, 0x180000
	s_addc_u32 s5, s5, 0
	s_add_u32 s6, s6, 0x300
	s_addc_u32 s7, s7, 0
.Lxq_no11a:
	s_waitcnt vmcnt(18)
	v_pk_mul_f32 v[8:9], v[8:9], v[56:57] op_sel_hi:[1,0]
	v_pk_mul_f32 v[10:11], v[10:11], v[56:57] op_sel_hi:[1,0]
	v_bfe_u32 v4, v8, 16, 1
	v_bfe_u32 v5, v9, 16, 1
	v_bfe_u32 v6, v10, 16, 1
	v_bfe_u32 v7, v11, 16, 1
	v_add3_u32 v8, v8, v4, s25
	v_add3_u32 v9, v9, v5, s25
	v_add3_u32 v10, v10, v6, s25
	v_add3_u32 v11, v11, v7, s25
	v_lshrrev_b32_e32 v8, 16, v8
	v_and_or_b32 v8, v9, s28, v8
	v_lshrrev_b32_e32 v10, 16, v10
	v_and_or_b32 v9, v11, s28, v10
	global_store_dwordx2 v1, v[8:9], s[26:27]
	s_add_u32 s26, s26, 0xc0000
	s_addc_u32 s27, s27, 0
	s_waitcnt vmcnt(17)
	v_pk_mul_f32 v[12:13], v[12:13], v[58:59] op_sel_hi:[1,0]
	v_pk_mul_f32 v[14:15], v[14:15], v[58:59] op_sel_hi:[1,0]
	v_bfe_u32 v4, v12, 16, 1
	v_bfe_u32 v5, v13, 16, 1
	v_bfe_u32 v6, v14, 16, 1
	v_bfe_u32 v7, v15, 16, 1
	v_add3_u32 v12, v12, v4, s25
	v_add3_u32 v13, v13, v5, s25
	v_add3_u32 v14, v14, v6, s25
	v_add3_u32 v15, v15, v7, s25
	v_lshrrev_b32_e32 v12, 16, v12
	v_and_or_b32 v12, v13, s28, v12
	v_lshrrev_b32_e32 v14, 16, v14
	v_and_or_b32 v13, v15, s28, v14
	global_store_dwordx2 v1, v[12:13], s[26:27]
	s_add_u32 s26, s26, 0xc0000
	s_addc_u32 s27, s27, 0
	s_waitcnt vmcnt(16)
	v_pk_mul_f32 v[16:17], v[16:17], v[60:61] op_sel_hi:[1,0]
	v_pk_mul_f32 v[18:19], v[18:19], v[60:61] op_sel_hi:[1,0]
	v_bfe_u32 v4, v16, 16, 1
	v_bfe_u32 v5, v17, 16, 1
	v_bfe_u32 v6, v18, 16, 1
	v_bfe_u32 v7, v19, 16, 1
	v_add3_u32 v16, v16, v4, s25
	v_add3_u32 v17, v17, v5, s25
	v_add3_u32 v18, v18, v6, s25
	v_add3_u32 v19, v19, v7, s25
	v_lshrrev_b32_e32 v16, 16, v16
	v_and_or_b32 v16, v17, s28, v16
	v_lshrrev_b32_e32 v18, 16, v18
	v_and_or_b32 v17, v19, s28, v18
	global_store_dwordx2 v1, v[16:17], s[26:27]
	s_add_u32 s26, s26, 0xc0000
	s_addc_u32 s27, s27, 0
	s_waitcnt vmcnt(15)
; #define GAS __attribute__((address_space(1)))
; __device__ __forceinline__ unsigned pk2(float lo, float hi) { return f2bf(lo) | (f2bf(hi) << 16); }
; __global__ void __launch_bounds__(NTHR, 2) fwd(Args args) {
;     ...
;             for (int i = gt; i < D * D / 4; i += NGT) { const int row = (i * 4) / D; const f32x4 w = ((const GAS f32x4*)INP(24))[i]; const float g = INP(22)[row]; v2u o; o.x = pk2(w.x * g, w.y * g); o.y = pk2(w.z * g, w.w * g);
;                 ((GAS v2u*)WSP(bf16, WS_WXQN))[i] = o; }
	v_pk_mul_f32 v[20:21], v[20:21], v[62:63] op_sel_hi:[1,0]
	v_pk_mul_f32 v[22:23], v[22:23], v[62:63] op_sel_hi:[1,0]
	v_bfe_u32 v4, v20, 16, 1
	v_bfe_u32 v5, v21, 16, 1
	v_bfe_u32 v6, v22, 16, 1
	v_bfe_u32 v7, v23, 16, 1
	v_add3_u32 v20, v20, v4, s25
	v_add3_u32 v21, v21, v5, s25
	v_add3_u32 v22, v22, v6, s25
	v_add3_u32 v23, v23, v7, s25
	v_lshrrev_b32_e32 v20, 16, v20
	v_and_or_b32 v20, v21, s28, v20
	v_lshrrev_b32_e32 v22, 16, v22
	v_and_or_b32 v21, v23, s28, v22
	global_store_dwordx2 v1, v[20:21], s[26:27]
	s_add_u32 s26, s26, 0xc0000
	s_addc_u32 s27, s27, 0
	s_waitcnt vmcnt(14)
	v_pk_mul_f32 v[24:25], v[24:25], v[64:65] op_sel_hi:[1,0]
	v_pk_mul_f32 v[26:27], v[26:27], v[64:65] op_sel_hi:[1,0]
	v_bfe_u32 v4, v24, 16, 1
	v_bfe_u32 v5, v25, 16, 1
	v_bfe_u32 v6, v26, 16, 1
	v_bfe_u32 v7, v27, 16, 1
	v_add3_u32 v24, v24, v4, s25
	v_add3_u32 v25, v25, v5, s25
	v_add3_u32 v26, v26, v6, s25
	v_add3_u32 v27, v27, v7, s25
	v_lshrrev_b32_e32 v24, 16, v24
	v_and_or_b32 v24, v25, s28, v24
	v_lshrrev_b32_e32 v26, 16, v26
	v_and_or_b32 v25, v27, s28, v26
	global_store_dwordx2 v1, v[24:25], s[26:27]
	s_add_u32 s26, s26, 0xc0000
	s_addc_u32 s27, s27, 0
	s_waitcnt vmcnt(13)
	v_pk_mul_f32 v[28:29], v[28:29], v[66:67] op_sel_hi:[1,0]
	v_pk_mul_f32 v[30:31], v[30:31], v[66:67] op_sel_hi:[1,0]
	v_bfe_u32 v4, v28, 16, 1
	v_bfe_u32 v5, v29, 16, 1
	v_bfe_u32 v6, v30, 16, 1
	v_bfe_u32 v7, v31, 16, 1
	v_add3_u32 v28, v28, v4, s25
	v_add3_u32 v29, v29, v5, s25
	v_add3_u32 v30, v30, v6, s25
	v_add3_u32 v31, v31, v7, s25
	v_lshrrev_b32_e32 v28, 16, v28
	v_and_or_b32 v28, v29, s28, v28
	v_lshrrev_b32_e32 v30, 16, v30
	v_and_or_b32 v29, v31, s28, v30
	global_store_dwordx2 v1, v[28:29], s[26:27]
	s_add_u32 s26, s26, 0xc0000
	s_addc_u32 s27, s27, 0
	s_waitcnt vmcnt(12)
	v_pk_mul_f32 v[32:33], v[32:33], v[68:69] op_sel_hi:[1,0]
	v_pk_mul_f32 v[34:35], v[34:35], v[68:69] op_sel_hi:[1,0]
	v_bfe_u32 v4, v32, 16, 1
	v_bfe_u32 v5, v33, 16, 1
	v_bfe_u32 v6, v34, 16, 1
	v_bfe_u32 v7, v35, 16, 1
	v_add3_u32 v32, v32, v4, s25
	v_add3_u32 v33, v33, v5, s25
	v_add3_u32 v34, v34, v6, s25
	v_add3_u32 v35, v35, v7, s25
	v_lshrrev_b32_e32 v32, 16, v32
	v_and_or_b32 v32, v33, s28, v32
	v_lshrrev_b32_e32 v34, 16, v34
	v_and_or_b32 v33, v35, s28, v34
	global_store_dwordx2 v1, v[32:33], s[26:27]
	s_add_u32 s26, s26, 0xc0000
	s_addc_u32 s27, s27, 0
	s_waitcnt vmcnt(11)
	v_pk_mul_f32 v[36:37], v[36:37], v[70:71] op_sel_hi:[1,0]
	v_pk_mul_f32 v[38:39], v[38:39], v[70:71] op_sel_hi:[1,0]
	v_bfe_u32 v4, v36, 16, 1
	v_bfe_u32 v5, v37, 16, 1
	v_bfe_u32 v6, v38, 16, 1
	v_bfe_u32 v7, v39, 16, 1
	v_add3_u32 v36, v36, v4, s25
	v_add3_u32 v37, v37, v5, s25
	v_add3_u32 v38, v38, v6, s25
	v_add3_u32 v39, v39, v7, s25
	v_lshrrev_b32_e32 v36, 16, v36
	v_and_or_b32 v36, v37, s28, v36
	v_lshrrev_b32_e32 v38, 16, v38
	v_and_or_b32 v37, v39, s28, v38
	global_store_dwordx2 v1, v[36:37], s[26:27]
	s_add_u32 s26, s26, 0xc0000
	s_addc_u32 s27, s27, 0
	s_waitcnt vmcnt(10)
	v_pk_mul_f32 v[40:41], v[40:41], v[72:73] op_sel_hi:[1,0]
	v_pk_mul_f32 v[42:43], v[42:43], v[72:73] op_sel_hi:[1,0]
	v_bfe_u32 v4, v40, 16, 1
	v_bfe_u32 v5, v41, 16, 1
	v_bfe_u32 v6, v42, 16, 1
	v_bfe_u32 v7, v43, 16, 1
	v_add3_u32 v40, v40, v4, s25
	v_add3_u32 v41, v41, v5, s25
	v_add3_u32 v42, v42, v6, s25
	v_add3_u32 v43, v43, v7, s25
	v_lshrrev_b32_e32 v40, 16, v40
	v_and_or_b32 v40, v41, s28, v40
	v_lshrrev_b32_e32 v42, 16, v42
	v_and_or_b32 v41, v43, s28, v42
	global_store_dwordx2 v1, v[40:41], s[26:27]
	s_add_u32 s26, s26, 0xc0000
	s_addc_u32 s27, s27, 0
	s_waitcnt vmcnt(9)
	v_pk_mul_f32 v[44:45], v[44:45], v[74:75] op_sel_hi:[1,0]
	v_pk_mul_f32 v[46:47], v[46:47], v[74:75] op_sel_hi:[1,0]
	v_bfe_u32 v4, v44, 16, 1
	v_bfe_u32 v5, v45, 16, 1
	v_bfe_u32 v6, v46, 16, 1
	v_bfe_u32 v7, v47, 16, 1
	v_add3_u32 v44, v44, v4, s25
	v_add3_u32 v45, v45, v5, s25
	v_add3_u32 v46, v46, v6, s25
	v_add3_u32 v47, v47, v7, s25
	v_lshrrev_b32_e32 v44, 16, v44
	v_and_or_b32 v44, v45, s28, v44
	v_lshrrev_b32_e32 v46, 16, v46
	v_and_or_b32 v45, v47, s28, v46
	global_store_dwordx2 v1, v[44:45], s[26:27]
	s_add_u32 s26, s26, 0xc0000
	s_addc_u32 s27, s27, 0
	s_cmp_lt_u32 s3, 128
	s_cbranch_scc0 .Lxq_no11b
	s_waitcnt vmcnt(10)
	v_pk_mul_f32 v[48:49], v[48:49], v[76:77] op_sel_hi:[1,0]
	v_pk_mul_f32 v[50:51], v[50:51], v[76:77] op_sel_hi:[1,0]
	v_bfe_u32 v4, v48, 16, 1
	v_bfe_u32 v5, v49, 16, 1
	v_bfe_u32 v6, v50, 16, 1
	v_bfe_u32 v7, v51, 16, 1
	v_add3_u32 v48, v48, v4, s25
	v_add3_u32 v49, v49, v5, s25
	v_add3_u32 v50, v50, v6, s25
	v_add3_u32 v51, v51, v7, s25
	v_lshrrev_b32_e32 v48, 16, v48
	v_and_or_b32 v48, v49, s28, v48
	v_lshrrev_b32_e32 v50, 16, v50
	v_and_or_b32 v49, v51, s28, v50
	global_store_dwordx2 v1, v[48:49], s[26:27]
	s_add_u32 s26, s26, 0xc0000
	s_addc_u32 s27, s27, 0
; #define GAS __attribute__((address_space(1)))
; template <bool GAIN, bool NT = false> __device__ __forceinline__ void titem8_load(const TItem& d, int lane, f32x4 (&r)[16], f32x4 (&g)[4]) {
;     const int q = lane & 7, kg = lane >> 3; const unsigned lo = (unsigned)((16 * kg) * d.N + 4 * q) * 4u;
;     const GAS char* base = (const GAS char*)d.src;
; #pragma unroll
;     for (int j = 0; j < 16; ++j) { const GAS f32x4* p = (const GAS f32x4*)(base + (size_t)j * (size_t)d.N * 4 + lo); r[j] = NT ? __builtin_nontemporal_load(p) : *p; }
;     if constexpr (GAIN) { const GAS char* gb = (const GAS char*)d.gain; const unsigned go = (unsigned)(16 * kg) * 4u;
; #pragma unroll
;         for (int j4 = 0; j4 < 4; ++j4) g[j4] = *(const GAS f32x4*)(gb + 16 * j4 + go); }
;     asm volatile("" ::: "memory"); __builtin_amdgcn_sched_barrier(0);
; }
.Lxq_no11b:
.LBB0_15:
	s_or_b64 exec, exec, s[0:1]
	s_lshl_b32 s0, s3, 3
	s_add_i32 s0, s89, s0
	s_lshl_b32 s4, s2, 3
	s_cmpk_lt_i32 s0, 0x400
	s_cselect_b64 s[6:7], -1, 0
	s_and_b64 vcc, exec, s[6:7]
	s_cbranch_vccz .LBB0_34
	s_ashr_i32 s1, s0, 31
	s_lshr_b32 s1, s1, 26
	s_add_i32 s1, s0, s1
	s_and_b32 s2, s1, 0x7ffffc0
	s_lshl_b32 s1, s1, 1
	s_and_b32 s26, s1, 0xffffff80
	s_ashr_i32 s27, s26, 31
	s_sub_i32 s5, s0, s2
	s_lshl_b64 s[2:3], s[26:27], 13
	s_add_u32 s1, s50, s2
	s_addc_u32 s25, s51, s3
	s_lshl_b32 s28, s5, 5
	s_ashr_i32 s29, s28, 31
	s_lshl_b64 s[2:3], s[28:29], 2
	v_lshlrev_b32_e32 v1, 2, v134
	s_add_u32 s30, s1, s2
	v_lshlrev_b32_e32 v0, 12, v134
	v_and_b32_e32 v34, 28, v1
	s_mov_b32 s1, 0x3fff8000
	v_and_or_b32 v0, v0, s1, v34
	s_addc_u32 s31, s25, s3
	v_lshlrev_b32_e32 v130, 2, v0
	v_mov_b32_e32 v131, 0
	v_lshl_add_u64 v[0:1], s[30:31], 0, v[130:131]
	s_movk_i32 s1, 0x2000
	v_add_co_u32_e32 v2, vcc, s1, v0
	s_movk_i32 s2, 0x4000
	s_nop 0
	v_addc_co_u32_e32 v3, vcc, 0, v1, vcc
	v_add_co_u32_e32 v8, vcc, s2, v0
	s_movk_i32 s3, 0x6000
	s_nop 0
	v_addc_co_u32_e32 v9, vcc, 0, v1, vcc
	global_load_dwordx4 v[4:7], v[2:3], off
	s_nop 0
	global_load_dwordx4 v[8:11], v[8:9], off
	v_add_co_u32_e32 v2, vcc, s3, v0
	s_mov_b32 s5, 0x8000
	s_nop 0
	v_addc_co_u32_e32 v3, vcc, 0, v1, vcc
	v_add_co_u32_e32 v16, vcc, s5, v0
	s_mov_b32 s25, 0xa000
	s_nop 0
	v_addc_co_u32_e32 v17, vcc, 0, v1, vcc
	global_load_dwordx4 v[12:15], v[2:3], off
	s_nop 0
	global_load_dwordx4 v[16:19], v[16:17], off
	v_add_co_u32_e32 v2, vcc, s25, v0
	s_mov_b32 s33, 0xc000
	s_nop 0
	v_addc_co_u32_e32 v3, vcc, 0, v1, vcc
	v_add_co_u32_e32 v24, vcc, s33, v0
	s_mov_b32 s36, 0xe000
	s_nop 0
	v_addc_co_u32_e32 v25, vcc, 0, v1, vcc
	global_load_dwordx4 v[20:23], v[2:3], off
	s_nop 0
	global_load_dwordx4 v[24:27], v[24:25], off
	v_add_co_u32_e32 v2, vcc, s36, v0
	s_mov_b32 s37, 0x10000
	s_nop 0
	v_addc_co_u32_e32 v3, vcc, 0, v1, vcc
	v_add_co_u32_e32 v32, vcc, s37, v0
	s_mov_b32 s38, 0x12000
	s_nop 0
	v_addc_co_u32_e32 v33, vcc, 0, v1, vcc
	global_load_dwordx4 v[28:31], v[2:3], off
	global_load_dwordx4 v[44:47], v[32:33], off
	v_add_co_u32_e32 v2, vcc, s38, v0
	s_mov_b32 s39, 0x14000
	s_nop 0
	v_addc_co_u32_e32 v3, vcc, 0, v1, vcc
	v_add_co_u32_e32 v32, vcc, s39, v0
	s_mov_b32 s40, 0x16000
	s_nop 0
	v_addc_co_u32_e32 v33, vcc, 0, v1, vcc
	global_load_dwordx4 v[56:59], v[2:3], off
	global_load_dwordx4 v[68:71], v[32:33], off
	v_add_co_u32_e32 v2, vcc, s40, v0
	s_mov_b32 s41, 0x18000
	s_nop 0
	v_addc_co_u32_e32 v3, vcc, 0, v1, vcc
	v_add_co_u32_e32 v32, vcc, s41, v0
	s_mov_b32 s42, 0x1a000
	s_nop 0
	v_addc_co_u32_e32 v33, vcc, 0, v1, vcc
	global_load_dwordx4 v[88:91], v[2:3], off
	global_load_dwordx4 v[100:103], v[32:33], off
	v_add_co_u32_e32 v2, vcc, s42, v0
	s_mov_b32 s43, 0x1c000
	s_nop 0
	v_addc_co_u32_e32 v3, vcc, 0, v1, vcc
	v_add_co_u32_e32 v32, vcc, s43, v0
	s_add_u32 s44, s78, 0x6b1c8000
	s_nop 0
	v_addc_co_u32_e32 v33, vcc, 0, v1, vcc
	v_add_co_u32_e32 v0, vcc, 0x1e000, v0
	global_load_dwordx4 v[116:119], v[2:3], off
	global_load_dwordx4 v[124:127], v[32:33], off
	v_addc_co_u32_e32 v1, vcc, 0, v1, vcc
	global_load_dwordx4 v[72:75], v130, s[30:31]
	global_load_dwordx4 v[36:39], v[0:1], off
	s_addc_u32 s45, s79, 0
	s_lshl_b64 s[28:29], s[28:29], 11
	s_add_u32 s28, s44, s28
	s_addc_u32 s29, s45, s29
	s_add_u32 s30, s28, s26
	s_addc_u32 s31, s29, s27
	s_mov_b32 s27, 0x1e000
	v_lshlrev_b32_e32 v0, 1, v134
	s_add_i32 s26, s0, s4
	v_and_b32_e32 v0, -16, v0
	s_cmpk_gt_i32 s26, 0x3ff
	v_lshl_add_u32 v128, v34, 11, v0
	v_mov_b32_e32 v129, v131
	s_cbranch_scc1 .LBB0_96
	s_lshl_b32 s26, s83, 3
	s_add_i32 s46, s89, s26
	s_lshl_b32 s26, s83, 4
	s_add_i32 s48, s89, s26
	s_addk_i32 s46, 0xfc00
	s_mov_b32 s86, s92
	s_lshl_b32 s51, s92, 3
	s_add_i32 s47, s26, 0xfffffc00
	s_addk_i32 s48, 0xfa00
	s_mov_b32 s26, 0x43800000
	s_mov_b32 s49, 0xc3e00000
	s_movk_i32 s50, 0x1000
	v_mov_b32_e32 v133, 0x43e00000
	s_branch .LBB0_19
